# attention queues: next item's atomic kept in flight during the unit (prefetched dequeue); all-wave vmcnt(0) at queue loop heads dropped
# speedup vs baseline: 1.0079x; 1.0079x over previous
_Z10hybrid_fwd4Args:
	s_mov_b32 s100, 0
	s_load_dwordx8 s[76:83], s[0:1], 0x80
	s_load_dword s84, s[0:1], 0xb8
	s_load_dwordx2 s[92:93], s[0:1], 0xa0
	s_load_dwordx4 s[56:59], s[0:1], 0xa8
	v_readfirstlane_b32 s3, v0
	s_add_u32 s4, s0, 0xb8
	s_addc_u32 s5, s1, 0
	v_writelane_b32 v255, s3, 0
	v_writelane_b32 v255, s4, 1
	s_waitcnt lgkmcnt(0)
	s_and_b32 s3, s84, 7
	s_cmp_lg_u32 s3, 0
	v_writelane_b32 v255, s5, 2
	s_mov_b32 s87, s2
	s_mov_b32 s94, s2
	s_cbranch_scc0 .LBB0_110
	s_movk_i32 s2, 0x100
	v_cmp_gt_u32_e32 vcc, s2, v0
	s_and_saveexec_b64 s[2:3], vcc

.LBB0_475:
	s_barrier
	s_and_saveexec_b64 s[2:3], s[0:1]
	s_cbranch_execz .LBB0_479
	s_waitcnt lgkmcnt(0)
	s_cmp_eq_u32 s100, 1
	s_cbranch_scc1 .Lqp1_have
	s_waitcnt vmcnt(0)
	v_mov_b32_e32 v253, 1
	global_atomic_add v253, v3, v253, s[92:93] offset:256 sc0
	s_waitcnt vmcnt(0)
	s_branch .Lqp1_go
.Lqp1_have:
	s_waitcnt vmcnt(8)
.Lqp1_go:
	v_mov_b32_e32 v2, s43
	ds_write_b32 v2, v253
	s_waitcnt lgkmcnt(0)
	v_mov_b32_e32 v253, 1
	global_atomic_add v253, v3, v253, s[92:93] offset:256 sc0
.LBB0_479:
	s_or_b64 exec, exec, s[2:3]
	s_mov_b32 s100, 1
	s_waitcnt lgkmcnt(0)
	s_barrier
	ds_read_b32 v1, v205
	s_mov_b64 s[2:3], -1
	s_waitcnt lgkmcnt(0)
	v_cmp_le_i32_e32 vcc, s29, v1
	v_readfirstlane_b32 s4, v1
	s_cbranch_vccnz .LBB0_474
	s_add_i32 s2, s4, 0xfffffe00
	s_cmpk_gt_i32 s4, 0x1ff
	s_cselect_b32 s2, s2, s4
	s_ashr_i32 s3, s2, 31
	s_lshr_b32 s3, s3, 26
	s_add_i32 s3, s2, s3
	s_ashr_i32 s52, s3, 6
	s_andn2_b32 s3, s3, 63
	s_sub_i32 s2, s2, s3
	v_mov_b32_e32 v1, v0
	s_ashr_i32 s20, s2, 2
	s_lshl_b32 s2, s2, 1
	v_readfirstlane_b32 s56, v1
	s_ashr_i32 s50, s56, 6
	s_ashr_i32 s51, s56, 8
	s_and_b32 s55, s2, 6
	s_sub_i32 s54, 7, s52
	s_and_b32 s53, s50, 3
	s_add_i32 s3, s51, s55
	s_ashr_i32 s21, s20, 31
	s_lshl_b32 s2, s54, 8
	s_lshl_b32 s57, s53, 6
	s_lshl_b32 s18, s3, 6
	s_or_b32 s6, s57, s2
	s_lshl_b64 s[4:5], s[20:21], 20
	s_ashr_i32 s19, s18, 31
	s_add_u32 s4, s4, s18
	v_and_b32_e32 v230, 31, v1
	s_addc_u32 s5, s5, s19
	v_or_b32_e32 v2, s6, v230
	s_lshl_b64 s[22:23], s[4:5], 1
	v_or_b32_e32 v4, 32, v2
	s_add_u32 s4, s30, s22
	v_mov_b32_e32 v5, v3
	s_addc_u32 s5, s31, s23
	v_lshlrev_b64 v[6:7], 10, v[2:3]
	v_lshlrev_b64 v[4:5], 10, v[4:5]
	s_lshl_b32 s58, s20, 3
	v_lshl_add_u64 v[6:7], s[4:5], 0, v[6:7]
	v_lshl_add_u64 v[4:5], s[4:5], 0, v[4:5]
	s_add_i32 s4, s3, s58
	s_ashr_i32 s5, s4, 31
	v_bfe_u32 v229, v1, 5, 1
	s_lshl_b64 s[4:5], s[4:5], 13
	v_lshlrev_b32_e32 v8, 4, v229
	v_mov_b32_e32 v9, v3
	s_add_u32 s4, s33, s4
	v_lshl_add_u64 v[4:5], v[4:5], 0, v[8:9]
	s_addc_u32 s5, s34, s5
	v_lshl_add_u64 v[6:7], v[6:7], 0, v[8:9]
	v_lshl_add_u64 v[8:9], v[2:3], 2, s[4:5]
	global_load_dwordx4 v[162:165], v[4:5], off offset:96
	global_load_dwordx4 v[166:169], v[4:5], off offset:64
	global_load_dwordx4 v[170:173], v[6:7], off offset:96
	global_load_dwordx4 v[174:177], v[6:7], off offset:64
	global_load_dwordx4 v[178:181], v[4:5], off offset:32
	global_load_dwordx4 v[182:185], v[4:5], off
	global_load_dwordx4 v[186:189], v[6:7], off offset:32
	global_load_dwordx4 v[190:193], v[6:7], off
	global_load_dword v232, v[8:9], off offset:128
	global_load_dword v233, v[8:9], off
	s_or_b32 s24, s55, s58
	s_ashr_i32 s25, s24, 31
	s_add_i32 s59, s58, 0x80
	s_lshl_b64 s[26:27], s[24:25], 13
	s_add_u32 s26, s33, s26
	s_addc_u32 s27, s34, s27
	s_lshl_b64 s[60:61], s[24:25], 2
	s_add_u32 s60, s35, s60
	s_mov_b32 s5, s7
	s_addc_u32 s61, s38, s61
	s_or_b32 s4, s59, s55
	v_mov_b32_e32 v2, v3
	v_mov_b32_e32 v4, v3
	s_lshl_b64 s[4:5], s[4:5], 2
	s_add_u32 s4, s35, s4
	s_addc_u32 s5, s38, s5
	s_mov_b32 s3, s7
	v_lshlrev_b32_e32 v5, 8, v230
	v_mov_b32_e32 v234, 0
	s_waitcnt vmcnt(0)
	global_load_dword v2, v3, s[60:61]
	global_load_dword v4, v3, s[4:5]
	s_lshl_b64 s[4:5], s[2:3], 2
	s_add_u32 s2, s26, s4
	s_addc_u32 s3, s27, s5
	global_load_dword v6, v3, s[2:3]
	s_nop 0
	global_load_dword v5, v5, s[26:27] offset:252
	s_cmpk_gt_u32 s56, 0xff
	s_waitcnt vmcnt(2)
	v_mul_f32_e32 v2, v2, v4
	v_mul_f32_e32 v4, 0x4f800000, v2
	v_cmp_gt_f32_e32 vcc, s44, v2
	s_waitcnt vmcnt(0)
	v_sub_f32_e32 v5, v6, v5
	v_cndmask_b32_e32 v2, v2, v4, vcc
	v_sqrt_f32_e32 v4, v2
	s_nop 0
	v_add_u32_e32 v6, -1, v4
	v_add_u32_e32 v7, 1, v4
	v_fma_f32 v8, -v6, v4, v2
	v_fma_f32 v9, -v7, v4, v2
	v_cmp_ge_f32_e64 s[2:3], 0, v8
	s_nop 1
	v_cndmask_b32_e64 v4, v4, v6, s[2:3]
	v_cmp_lt_f32_e64 s[2:3], 0, v9
	s_nop 1
	v_cndmask_b32_e64 v4, v4, v7, s[2:3]
	v_mul_f32_e32 v6, 0x37800000, v4
	v_cndmask_b32_e32 v4, v4, v6, vcc
	v_cmp_class_f32_e32 vcc, v2, v226
	s_nop 1
	v_cndmask_b32_e32 v2, v4, v2, vcc
	v_fmac_f32_e32 v5, 2.0, v2
	v_cmp_le_f32_e32 vcc, s45, v5
	s_cbranch_scc1 .LBB0_482
	s_lshl_b64 s[2:3], s[6:7], 2
	s_add_u32 s2, s26, s2
	s_addc_u32 s3, s27, s3
	global_load_dword v4, v3, s[2:3]
	v_add_f32_e32 v2, v2, v2
	v_add_f32_e32 v2, 0x42480000, v2
	s_waitcnt vmcnt(0)
	v_add_f32_e32 v234, v2, v4

.LBB0_515:
	s_barrier
	s_and_saveexec_b64 s[2:3], s[0:1]
	s_cbranch_execz .LBB0_519
	s_waitcnt lgkmcnt(0)
	s_cmp_eq_u32 s100, 2
	s_cbranch_scc1 .Lqp2_have
	s_waitcnt vmcnt(0)
	v_mov_b32_e32 v253, 1
	global_atomic_add v253, v3, v253, s[92:93] offset:1024 sc0
	s_waitcnt vmcnt(0)
	s_branch .Lqp2_go

.Lqp2_go:
	v_mov_b32_e32 v4, s24
	ds_write_b32 v4, v253
	s_waitcnt lgkmcnt(0)
	v_mov_b32_e32 v253, 1
	global_atomic_add v253, v3, v253, s[92:93] offset:1024 sc0
.LBB0_519:
	s_or_b64 exec, exec, s[2:3]
	s_mov_b32 s100, 2
	s_waitcnt lgkmcnt(0)
	s_barrier
	ds_read_b32 v2, v1
	s_mov_b64 s[2:3], -1
	s_waitcnt lgkmcnt(0)
	v_cmp_le_i32_e32 vcc, s29, v2
	v_readfirstlane_b32 s6, v2
	s_cbranch_vccnz .LBB0_514
	s_add_i32 s2, s6, 0xfffffe00
	s_cmpk_gt_i32 s6, 0x1ff
	s_cselect_b32 s2, s2, s6
	s_ashr_i32 s3, s2, 31
	s_lshr_b32 s3, s3, 26
	v_mov_b32_e32 v10, v0
	s_add_i32 s3, s2, s3
	s_ashr_i32 s42, s3, 6
	v_readfirstlane_b32 s34, v10
	s_andn2_b32 s3, s3, 63
	s_ashr_i32 s31, s34, 6
	s_sub_i32 s6, 7, s42
	s_sub_i32 s12, s2, s3
	s_and_b32 s13, s31, 3
	s_and_b32 s2, s12, 3
	s_ashr_i32 s14, s34, 8
	s_lshl_b32 s3, s6, 8
	s_lshl_b32 s43, s13, 6
	s_ashr_i32 s10, s12, 2
	s_or_b32 s30, s43, s3
	s_lshl_b32 s2, s2, 7
	s_lshl_b32 s3, s14, 6
	s_ashr_i32 s11, s10, 31
	s_add_i32 s2, s3, s2
	s_ashr_i32 s3, s2, 31
	s_lshl_b64 s[8:9], s[10:11], 21
	v_and_b32_e32 v203, 31, v10
	s_add_u32 s15, s18, s8
	v_or_b32_e32 v2, s30, v203
	s_addc_u32 s16, s19, s9
	s_lshl_b64 s[8:9], s[2:3], 1
	v_or_b32_e32 v4, 32, v2
	s_add_u32 s2, s15, s8
	v_mov_b32_e32 v5, v3
	v_bfe_u32 v202, v10, 5, 1
	s_addc_u32 s3, s16, s9
	v_lshlrev_b64 v[4:5], 10, v[4:5]
	v_lshlrev_b64 v[6:7], 10, v[2:3]
	v_lshlrev_b32_e32 v2, 4, v202
	v_lshl_add_u64 v[4:5], s[2:3], 0, v[4:5]
	v_lshl_add_u64 v[6:7], s[2:3], 0, v[6:7]
	v_lshl_add_u64 v[4:5], v[4:5], 0, v[2:3]
	v_lshl_add_u64 v[6:7], v[6:7], 0, v[2:3]
	global_load_dwordx4 v[162:165], v[4:5], off offset:96
	global_load_dwordx4 v[166:169], v[4:5], off offset:64
	global_load_dwordx4 v[170:173], v[6:7], off offset:96
	global_load_dwordx4 v[174:177], v[6:7], off offset:64
	global_load_dwordx4 v[178:181], v[4:5], off offset:32
	global_load_dwordx4 v[182:185], v[4:5], off
	global_load_dwordx4 v[186:189], v[6:7], off offset:32
	global_load_dwordx4 v[190:193], v[6:7], off
	s_lshl_b32 s40, s6, 2
	s_add_i32 s2, s40, -8
	s_cmp_gt_u32 s6, 2
	s_cselect_b32 s6, s2, 0
	s_lshl_b32 s12, s12, 6
	s_lshl_b64 s[2:3], s[10:11], 19
	s_and_b32 s12, s12, 0x80
	v_lshlrev_b32_e32 v6, 6, v10
	s_or_b32 s2, s2, s12
	v_and_b32_e32 v6, 0xf00, v6
	s_add_u32 s12, s20, s2
	v_and_b32_e32 v205, 63, v10
	v_lshl_or_b32 v6, s13, 12, v6
	s_addc_u32 s13, s21, s3
	v_mov_b32_e32 v5, v3
	v_lshlrev_b32_e32 v4, 8, v205
	s_add_u32 s2, s22, s2
	v_mov_b32_e32 v7, v3
	v_lshlrev_b32_e32 v204, 3, v10
	v_lshl_add_u64 v[4:5], s[12:13], 0, v[4:5]
	s_addc_u32 s3, s23, s3
	s_lshl_b32 s12, s31, 3
	s_lshl_b32 s14, s14, 5
	v_and_b32_e32 v15, 24, v204
	s_lshl_b32 s33, s31, 10
	s_ashr_i32 s13, s12, 31
	v_lshl_add_u64 v[6:7], s[2:3], 0, v[6:7]
	s_ashr_i32 s15, s14, 31
	v_mov_b32_e32 v9, v3
	v_lshlrev_b32_e32 v8, 1, v15
	s_lshl_b64 s[16:17], s[6:7], 14
	s_add_i32 s33, s33, 0
	v_lshl_add_u64 v[194:195], s[12:13], 1, v[4:5]
	v_lshl_add_u64 v[4:5], s[14:15], 1, v[6:7]
	v_mov_b32_e32 v11, v3
	v_mov_b32_e32 v12, v3
	v_mov_b32_e32 v13, v3
	v_mov_b32_e32 v14, v3
	s_add_i32 s2, s33, 0x8000
	v_lshl_add_u64 v[196:197], v[4:5], 0, v[8:9]
	v_lshl_add_u64 v[4:5], v[194:195], 0, s[16:17]
	s_mov_b32 m0, s33
	v_lshl_add_u64 v[6:7], v[196:197], 0, s[16:17]
	v_lshlrev_b32_e32 v206, 2, v202
	s_lshl_b32 s41, s6, 6
	v_mov_b32_e32 v16, v3
	v_mov_b32_e32 v17, v3
	v_mov_b32_e32 v8, v3
	v_mov_b32_e32 v211, 0
	s_add_i32 s35, s30, 0xfffffe00
	s_add_i32 s38, s30, 0xfffffe1f
	s_add_i32 s39, s30, 0xfffffe3f
	s_or_b32 s40, s40, 3
	s_waitcnt vmcnt(0)
	s_barrier
	global_load_lds_dwordx4 v[4:5], off
	s_mov_b32 m0, s2
	s_and_b32 s2, s34, 0x3fffffc0
	global_load_lds_dwordx4 v[6:7], off
	s_lshl_b32 s2, s2, 2
	s_add_i32 s2, s2, 0
	s_add_i32 s12, s2, 0x10400
	v_lshlrev_b32_e32 v4, 1, v10
	v_lshrrev_b32_e32 v5, 2, v10
	v_lshl_add_u32 v200, v203, 2, s12
	v_add_u32_e32 v199, s12, v2
	s_lshl_b32 s12, s42, 8
	v_and_b32_e32 v4, 32, v4
	v_and_or_b32 v5, v5, 3, v206
	s_sub_i32 s12, s43, s12
	v_lshlrev_b32_e32 v5, 6, v5
	v_add_u32_e32 v2, 0, v4
	s_addk_i32 s12, 0x700
	v_add3_u32 v208, v2, v5, v15
	v_or_b32_e32 v2, s12, v203
	s_waitcnt vmcnt(0)
	v_lshlrev_b32_e32 v6, 10, v202
	v_lshlrev_b32_e32 v7, 4, v203
	v_sub_u32_e32 v2, v2, v206
	v_add3_u32 v207, 0, v6, v7
	v_subrev_u32_e32 v209, s41, v2
	v_mov_b32_e32 v2, v3
	v_mov_b32_e32 v4, v3
	v_mov_b32_e32 v5, v3
	v_mov_b32_e32 v6, v3
	v_mov_b32_e32 v7, v3
	v_mov_b32_e32 v10, v3
	v_mov_b32_e32 v11, v3
	v_mov_b32_e32 v12, v3
	v_mov_b32_e32 v13, v3
	v_mov_b32_e32 v14, v3
	v_mov_b32_e32 v15, v3
	v_mov_b64_e32 v[64:65], v[16:17]
	v_mov_b64_e32 v[80:81], v[16:17]
	v_mov_b64_e32 v[32:33], v[16:17]
	v_mov_b64_e32 v[48:49], v[16:17]
	s_or_b32 s34, s30, 63
	v_cmp_gt_u32_e64 s[2:3], 32, v205
	v_mov_b64_e32 v[62:63], v[14:15]
	v_mov_b64_e32 v[60:61], v[12:13]
	v_mov_b64_e32 v[58:59], v[10:11]
	v_mov_b64_e32 v[56:57], v[8:9]
	v_mov_b64_e32 v[54:55], v[6:7]
	v_mov_b64_e32 v[52:53], v[4:5]
	v_mov_b64_e32 v[50:51], v[2:3]
	v_mov_b64_e32 v[78:79], v[14:15]
	v_mov_b64_e32 v[76:77], v[12:13]
	v_mov_b64_e32 v[74:75], v[10:11]
	v_mov_b64_e32 v[72:73], v[8:9]
	v_mov_b64_e32 v[70:71], v[6:7]
	v_mov_b64_e32 v[68:69], v[4:5]
	v_mov_b64_e32 v[66:67], v[2:3]
	v_mov_b64_e32 v[30:31], v[14:15]
	v_mov_b64_e32 v[28:29], v[12:13]
	v_mov_b64_e32 v[26:27], v[10:11]
	v_mov_b64_e32 v[24:25], v[8:9]
	v_mov_b64_e32 v[22:23], v[6:7]
	v_mov_b64_e32 v[20:21], v[4:5]
	v_mov_b64_e32 v[18:19], v[2:3]
	v_mov_b64_e32 v[46:47], v[14:15]
	v_mov_b64_e32 v[44:45], v[12:13]
	v_mov_b64_e32 v[42:43], v[10:11]
	v_mov_b64_e32 v[40:41], v[8:9]
	v_mov_b64_e32 v[38:39], v[6:7]
	v_mov_b64_e32 v[36:37], v[4:5]
	v_mov_b64_e32 v[34:35], v[2:3]
	v_mov_b32_e32 v210, 0
	v_mov_b32_e32 v212, 0
	v_mov_b32_e32 v201, 0
	s_mov_b32 s12, s6
	v_mov_b32_e32 v82, 0
	v_mov_b32_e32 v83, v211
	v_mov_b32_e32 v84, v211
	v_mov_b32_e32 v85, v211
	v_mov_b32_e32 v86, v211
	v_mov_b32_e32 v87, v211
	v_mov_b32_e32 v88, v211
	v_mov_b32_e32 v89, v211
	v_mov_b32_e32 v90, v211
	v_mov_b32_e32 v91, v211
	v_mov_b32_e32 v92, v211
	v_mov_b32_e32 v93, v211
	v_mov_b32_e32 v94, v211
	v_mov_b32_e32 v95, v211
	v_mov_b32_e32 v96, v211
	v_mov_b32_e32 v97, v211
	s_waitcnt vmcnt(0) lgkmcnt(0)
	s_barrier
	s_branch .LBB0_524

.LBB0_549:
	s_barrier
	s_and_saveexec_b64 s[10:11], s[0:1]
	s_cbranch_execz .LBB0_553
	s_waitcnt lgkmcnt(0)
	s_cmp_eq_u32 s100, 3
	s_cbranch_scc1 .Lqp3_have
	s_waitcnt vmcnt(0)
	v_mov_b32_e32 v253, 1
	global_atomic_add v253, v77, v253, s[92:93] offset:1280 sc0
	s_waitcnt vmcnt(0)
	s_branch .Lqp3_go
.Lqp3_have:
	s_waitcnt vmcnt(4)
.Lqp3_go:
	v_mov_b32_e32 v3, s25
	ds_write_b32 v3, v253
	s_waitcnt lgkmcnt(0)
	v_mov_b32_e32 v253, 1
	global_atomic_add v253, v77, v253, s[92:93] offset:1280 sc0
.LBB0_553:
	s_or_b64 exec, exec, s[10:11]
	s_mov_b32 s100, 3
	v_mov_b32_e32 v2, s25
	s_waitcnt lgkmcnt(0)
	s_barrier
	ds_read_b32 v2, v2
	s_mov_b64 s[10:11], -1
	s_waitcnt lgkmcnt(0)
	v_readfirstlane_b32 s14, v2
	s_cmp_ge_i32 s14, s18
	s_cbranch_scc1 .LBB0_548
	s_add_i32 s10, s14, 0xfffffc00
	s_cmpk_gt_i32 s14, 0x3ff
	s_cselect_b32 s33, s10, s14
	s_ashr_i32 s10, s33, 6
	s_ashr_i32 s11, s10, 31
	s_bfe_u32 s14, s33, 0x10005
	v_readfirstlane_b32 s31, v0
	s_lshl_b64 s[16:17], s[10:11], 11
	s_lshl_b32 s10, s10, 1
	s_and_b32 s30, s33, 31
	s_lshr_b32 s39, s31, 6
	s_lshl_b32 s38, s14, 2
	s_or_b32 s14, s10, s14
	s_lshl_b32 s34, s30, 6
	s_lshl_b32 s35, s39, 3
	s_ashr_i32 s15, s14, 31
	s_add_i32 s29, s35, s34
	s_lshl_b64 s[10:11], s[14:15], 14
	s_add_u32 s40, s19, s10
	s_addc_u32 s41, s20, s11
	s_add_u32 s42, s21, s10
	s_addc_u32 s43, s22, s11
	s_lshl_b32 s10, s39, 4
	s_add_u32 s10, s40, s10
	s_addc_u32 s11, s41, 0
	s_lshr_b32 s31, s31, 2
	v_or_b32_e32 v76, s29, v67
	v_and_or_b32 v14, s31, 48, v71
	s_and_b32 s31, s31, 0x3fffffc0
	v_lshl_add_u64 v[2:3], s[16:17], 0, v[76:77]
	s_add_u32 s40, s42, s31
	v_or_b32_e32 v4, s38, v69
	v_lshlrev_b64 v[2:3], 10, v[2:3]
	s_addc_u32 s41, s43, 0
	v_mov_b32_e32 v89, v77
	v_mov_b32_e32 v91, v77
	v_lshl_add_u64 v[2:3], s[12:13], 0, v[2:3]
	v_lshlrev_b32_e32 v4, 7, v4
	v_mov_b32_e32 v5, v77
	v_lshl_add_u64 v[10:11], s[40:41], 0, v[88:89]
	v_lshl_add_u64 v[12:13], s[10:11], 0, v[90:91]
	v_lshlrev_b32_e32 v14, 7, v14
	v_mov_b32_e32 v15, v77
	v_lshl_add_u64 v[2:3], v[2:3], 0, v[4:5]
	v_mov_b32_e32 v87, v77
	v_lshl_add_u64 v[18:19], v[10:11], 0, v[14:15]
	v_add_co_u32_e32 v14, vcc, s26, v12
	v_lshl_add_u64 v[6:7], v[2:3], 0, v[86:87]
	s_nop 0
	v_addc_co_u32_e32 v15, vcc, 0, v13, vcc
	global_load_dwordx4 v[2:5], v[6:7], off
	global_load_dwordx4 v[92:95], v[6:7], off offset:32
	global_load_dwordx4 v[182:185], v[6:7], off offset:64
	global_load_dwordx4 v[186:189], v[6:7], off offset:96
	s_barrier
	global_load_dwordx4 v[6:9], v90, s[10:11]
	global_load_dwordx4 v[10:13], v[18:19], off
	s_nop 0
	global_load_dwordx4 v[14:17], v[14:15], off
	v_add_co_u32_e32 v18, vcc, s26, v18
	s_lshl_b32 s31, s39, 10
	s_nop 0
	v_addc_co_u32_e32 v19, vcc, 0, v19, vcc
	global_load_dwordx4 v[18:21], v[18:19], off
	v_add_u32_e32 v22, s31, v73
	v_subrev_co_u32_e64 v76, s[10:11], 31, v76
	v_lshrrev_b32_e32 v87, 4, v76
	v_add_u32_e32 v87, 1, v87
	v_cmp_gt_u32_e32 vcc, s27, v76
	v_mov_b32_e32 v203, v77
	s_waitcnt vmcnt(3)
	ds_write_b128 v22, v[6:9]
	s_waitcnt vmcnt(2)
	ds_write_b128 v22, v[10:13] offset:16384
	s_waitcnt vmcnt(1)
	ds_write_b128 v22, v[14:17] offset:8192
	s_waitcnt vmcnt(0)
	ds_write_b128 v22, v[18:21] offset:24576
	s_waitcnt lgkmcnt(0)
	s_barrier
	ds_read_b128 v[6:9], v177
	ds_read_b128 v[10:13], v177 offset:512
	s_waitcnt lgkmcnt(1)
	v_mfma_f32_32x32x16_bf16 v[50:65], v[6:9], v[2:5], 0
	v_cndmask_b32_e32 v76, v180, v87, vcc
	v_cndmask_b32_e64 v76, v76, 0, s[10:11]
	v_cmp_lt_u32_e32 vcc, v75, v76
	s_waitcnt lgkmcnt(0)
	v_mfma_f32_32x32x16_bf16 v[34:49], v[10:13], v[2:5], 0
	ds_read_b128 v[6:9], v177 offset:8192
	ds_read_b128 v[10:13], v177 offset:8704
	ds_read_b128 v[190:193], v177 offset:2048
	ds_read_b128 v[194:197], v177 offset:2560
	s_waitcnt lgkmcnt(3)
	v_mfma_f32_32x32x16_bf16 v[18:33], v[6:9], v[2:5], 0
	s_waitcnt lgkmcnt(2)
	v_mfma_f32_32x32x16_bf16 v[2:17], v[10:13], v[2:5], 0
	s_waitcnt lgkmcnt(1)
	v_mfma_f32_32x32x16_bf16 v[50:65], v[190:193], v[92:95], v[50:65]
	s_waitcnt lgkmcnt(0)
	v_mfma_f32_32x32x16_bf16 v[34:49], v[194:197], v[92:95], v[34:49]
	ds_read_b128 v[190:193], v177 offset:10240
	ds_read_b128 v[194:197], v177 offset:10752
	s_waitcnt lgkmcnt(1)
	v_mfma_f32_32x32x16_bf16 v[18:33], v[190:193], v[92:95], v[18:33]
	s_waitcnt lgkmcnt(0)
	v_mfma_f32_32x32x16_bf16 v[2:17], v[194:197], v[92:95], v[2:17]
	ds_read_b128 v[92:95], v177 offset:4096
	ds_read_b128 v[190:193], v177 offset:4608
	s_waitcnt lgkmcnt(1)
	v_mfma_f32_32x32x16_bf16 v[50:65], v[92:95], v[182:185], v[50:65]
	s_waitcnt lgkmcnt(0)
	v_mfma_f32_32x32x16_bf16 v[34:49], v[190:193], v[182:185], v[34:49]
	ds_read_b128 v[92:95], v177 offset:12288
	ds_read_b128 v[190:193], v177 offset:12800
	s_waitcnt lgkmcnt(1)
	v_mfma_f32_32x32x16_bf16 v[18:33], v[92:95], v[182:185], v[18:33]
	s_waitcnt lgkmcnt(0)
	v_mfma_f32_32x32x16_bf16 v[2:17], v[190:193], v[182:185], v[2:17]
	ds_read_b128 v[92:95], v177 offset:6144
	ds_read_b128 v[182:185], v177 offset:6656
	s_waitcnt lgkmcnt(1)
	v_mfma_f32_32x32x16_bf16 v[50:65], v[92:95], v[186:189], v[50:65]
	s_waitcnt lgkmcnt(0)
	v_mfma_f32_32x32x16_bf16 v[34:49], v[182:185], v[186:189], v[34:49]
	s_nop 9
	v_cndmask_b32_e32 v50, v178, v50, vcc
	v_cmp_lt_u32_e32 vcc, v81, v76
	ds_read_b128 v[92:95], v177 offset:14336
	ds_read_b128 v[182:185], v177 offset:14848
	v_cndmask_b32_e32 v51, v178, v51, vcc
	v_cmp_lt_u32_e32 vcc, v83, v76
	s_nop 1
	v_cndmask_b32_e32 v52, v178, v52, vcc
	v_cmp_lt_u32_e32 vcc, v85, v76
	s_waitcnt lgkmcnt(1)
	v_mfma_f32_32x32x16_bf16 v[18:33], v[92:95], v[186:189], v[18:33]
	v_cndmask_b32_e32 v53, v178, v53, vcc
	v_cmp_lt_u32_e32 vcc, v98, v76
	s_nop 1
	v_cndmask_b32_e32 v54, v178, v54, vcc
	v_cmp_lt_u32_e32 vcc, v99, v76
	s_waitcnt lgkmcnt(0)
	v_mfma_f32_32x32x16_bf16 v[2:17], v[182:185], v[186:189], v[2:17]
	v_cndmask_b32_e32 v55, v178, v55, vcc
	v_cmp_lt_u32_e32 vcc, v100, v76
	s_nop 1
	v_cndmask_b32_e32 v56, v178, v56, vcc
	v_cmp_lt_u32_e32 vcc, v101, v76
	s_nop 1
	v_cndmask_b32_e32 v57, v178, v57, vcc
	v_cmp_lt_u32_e32 vcc, v102, v76
	s_nop 1
	v_cndmask_b32_e32 v58, v178, v58, vcc
	v_cmp_lt_u32_e32 vcc, v103, v76
	s_nop 1
	v_cndmask_b32_e32 v59, v178, v59, vcc
	v_cmp_lt_u32_e32 vcc, v104, v76
	s_nop 1
	v_cndmask_b32_e32 v60, v178, v60, vcc
	v_cmp_lt_u32_e32 vcc, v105, v76
	s_nop 1
	v_cndmask_b32_e32 v61, v178, v61, vcc
	v_cmp_lt_u32_e32 vcc, v106, v76
	s_nop 1
	v_cndmask_b32_e32 v62, v178, v62, vcc
	v_cmp_lt_u32_e32 vcc, v107, v76
	s_nop 1
	v_cndmask_b32_e32 v63, v178, v63, vcc
	v_cmp_lt_u32_e32 vcc, v108, v76
	s_nop 1
	v_cndmask_b32_e32 v64, v178, v64, vcc
	v_cmp_lt_u32_e32 vcc, v109, v76
	s_nop 1
	v_cndmask_b32_e32 v65, v178, v65, vcc
	v_cmp_lt_u32_e32 vcc, v110, v76
	s_nop 1
	v_cndmask_b32_e32 v34, v178, v34, vcc
	v_cmp_lt_u32_e32 vcc, v111, v76
	s_nop 1
	v_cndmask_b32_e32 v35, v178, v35, vcc
	v_cmp_lt_u32_e32 vcc, v112, v76
	s_nop 1
	v_cndmask_b32_e32 v36, v178, v36, vcc
	v_cmp_lt_u32_e32 vcc, v113, v76
	s_nop 1
	v_cndmask_b32_e32 v37, v178, v37, vcc
	v_cmp_lt_u32_e32 vcc, v114, v76
	s_nop 1
	v_cndmask_b32_e32 v38, v178, v38, vcc
	v_cmp_lt_u32_e32 vcc, v115, v76
	s_nop 1
	v_cndmask_b32_e32 v39, v178, v39, vcc
	v_cmp_lt_u32_e32 vcc, v116, v76
	s_nop 1
	v_cndmask_b32_e32 v40, v178, v40, vcc
	v_cmp_lt_u32_e32 vcc, v117, v76
	s_nop 1
	v_cndmask_b32_e32 v41, v178, v41, vcc
	v_cmp_lt_u32_e32 vcc, v118, v76
	s_nop 1
	v_cndmask_b32_e32 v42, v178, v42, vcc
	v_cmp_lt_u32_e32 vcc, v119, v76
	s_nop 1
	v_cndmask_b32_e32 v43, v178, v43, vcc
	v_cmp_lt_u32_e32 vcc, v120, v76
	s_nop 1
	v_cndmask_b32_e32 v44, v178, v44, vcc
	v_cmp_lt_u32_e32 vcc, v121, v76
	s_nop 1
	v_cndmask_b32_e32 v45, v178, v45, vcc
	v_cmp_lt_u32_e32 vcc, v122, v76
	s_nop 1
	v_cndmask_b32_e32 v46, v178, v46, vcc
	v_cmp_lt_u32_e32 vcc, v123, v76
	s_nop 1
	v_cndmask_b32_e32 v47, v178, v47, vcc
	v_cmp_lt_u32_e32 vcc, v124, v76
	s_nop 1
	v_cndmask_b32_e32 v48, v178, v48, vcc
	v_cmp_lt_u32_e32 vcc, v125, v76
	s_nop 1
	v_cndmask_b32_e32 v49, v178, v49, vcc
	v_cmp_lt_u32_e32 vcc, v126, v76
	s_nop 1
	v_cndmask_b32_e32 v87, v178, v18, vcc
	v_cmp_lt_u32_e32 vcc, v127, v76
	s_nop 1
	v_cndmask_b32_e32 v89, v178, v19, vcc
	v_cmp_lt_u32_e32 vcc, v128, v76
	s_nop 1
	v_cndmask_b32_e32 v91, v178, v20, vcc
	v_cmp_lt_u32_e32 vcc, v129, v76
	s_nop 1
	v_cndmask_b32_e32 v92, v178, v21, vcc
	v_cmp_lt_u32_e32 vcc, v130, v76
	s_nop 1
	v_cndmask_b32_e32 v93, v178, v22, vcc
	v_cmp_lt_u32_e32 vcc, v131, v76
	s_nop 1
	v_cndmask_b32_e32 v94, v178, v23, vcc
	v_cmp_lt_u32_e32 vcc, v132, v76
	s_nop 1
	v_cndmask_b32_e32 v24, v178, v24, vcc
	v_cmp_lt_u32_e32 vcc, v133, v76
	s_nop 1
	v_cndmask_b32_e32 v25, v178, v25, vcc
	v_cmp_lt_u32_e32 vcc, v134, v76
	s_nop 1
	v_cndmask_b32_e32 v26, v178, v26, vcc
	v_cmp_lt_u32_e32 vcc, v135, v76
	s_nop 1
	v_cndmask_b32_e32 v27, v178, v27, vcc
	v_cmp_lt_u32_e32 vcc, v136, v76
	s_nop 1
	v_cndmask_b32_e32 v95, v178, v28, vcc
	v_cmp_lt_u32_e32 vcc, v137, v76
	s_nop 1
	v_cndmask_b32_e32 v96, v178, v29, vcc
	v_cmp_lt_u32_e32 vcc, v138, v76
	s_nop 1
	v_cndmask_b32_e32 v97, v178, v30, vcc
	v_cmp_lt_u32_e32 vcc, v139, v76
	s_nop 1
	v_cndmask_b32_e32 v183, v178, v31, vcc
	v_cmp_lt_u32_e32 vcc, v140, v76
	s_nop 1
	v_cndmask_b32_e32 v32, v178, v32, vcc
	v_cmp_lt_u32_e32 vcc, v141, v76
	s_nop 1
	v_cndmask_b32_e32 v33, v178, v33, vcc
	v_cmp_lt_u32_e32 vcc, v142, v76
	s_nop 1
	v_cndmask_b32_e32 v186, v178, v2, vcc
	v_cmp_lt_u32_e32 vcc, v143, v76
	v_max3_f32 v2, v178, v50, v51
	s_nop 0
	v_max3_f32 v2, v2, v54, v55
	s_nop 0
	v_cndmask_b32_e32 v187, v178, v3, vcc
	v_max3_f32 v3, v178, v52, v53
	v_cmp_lt_u32_e32 vcc, v144, v76
	v_max3_f32 v3, v3, v56, v57
	v_max3_f32 v2, v2, v58, v59
	s_nop 0
	v_max3_f32 v3, v3, v60, v61
	v_max3_f32 v2, v2, v62, v63
	s_nop 0
	v_cndmask_b32_e32 v188, v178, v4, vcc
	v_cmp_lt_u32_e32 vcc, v145, v76
	v_max3_f32 v3, v3, v64, v65
	v_max3_f32 v2, v2, v34, v35
	s_nop 0
	v_max3_f32 v3, v3, v36, v37
	v_max3_f32 v2, v2, v38, v39
	s_nop 0
	v_cndmask_b32_e32 v189, v178, v5, vcc
	v_cmp_lt_u32_e32 vcc, v146, v76
	v_max3_f32 v3, v3, v40, v41
	v_max3_f32 v2, v2, v42, v43
	s_nop 0
	v_max3_f32 v3, v3, v44, v45
	v_max3_f32 v2, v2, v46, v47
	s_nop 0
	v_cndmask_b32_e32 v190, v178, v6, vcc
	v_cmp_lt_u32_e32 vcc, v147, v76
	v_max3_f32 v3, v3, v48, v49
	v_max3_f32 v2, v2, v87, v89
	s_nop 0
	v_max3_f32 v3, v3, v91, v92
	v_max3_f32 v2, v2, v93, v94
	s_nop 0
	v_cndmask_b32_e32 v191, v178, v7, vcc
	v_cmp_lt_u32_e32 vcc, v148, v76
	v_max3_f32 v3, v3, v24, v25
	v_max3_f32 v2, v2, v26, v27
	s_nop 0
	v_max3_f32 v3, v3, v95, v96
	v_max3_f32 v2, v2, v97, v183
	s_nop 0
	v_cndmask_b32_e32 v8, v178, v8, vcc
	v_cmp_lt_u32_e32 vcc, v149, v76
	v_max3_f32 v3, v3, v32, v33
	v_max3_f32 v2, v2, v186, v187
	s_nop 0
	v_max3_f32 v3, v3, v188, v189
	v_max3_f32 v2, v2, v190, v191
	s_nop 0
	v_cndmask_b32_e32 v9, v178, v9, vcc
	v_cmp_lt_u32_e32 vcc, v150, v76
	v_max3_f32 v3, v3, v8, v9
	s_nop 1
	v_cndmask_b32_e32 v10, v178, v10, vcc
	v_cmp_lt_u32_e32 vcc, v151, v76
	s_nop 1
	v_cndmask_b32_e32 v11, v178, v11, vcc
	v_cmp_lt_u32_e32 vcc, v152, v76
	v_max3_f32 v2, v2, v10, v11
	s_nop 1
	v_cndmask_b32_e32 v196, v178, v12, vcc
	v_cmp_lt_u32_e32 vcc, v153, v76
	s_nop 1
	v_cndmask_b32_e32 v197, v178, v13, vcc
	v_cmp_lt_u32_e32 vcc, v154, v76
	v_max3_f32 v3, v3, v196, v197
	s_nop 1
	v_cndmask_b32_e32 v198, v178, v14, vcc
	v_cmp_lt_u32_e32 vcc, v155, v76
	s_nop 1
	v_cndmask_b32_e32 v199, v178, v15, vcc
	v_cmp_lt_u32_e32 vcc, v156, v76
	v_max3_f32 v2, v2, v198, v199
	s_nop 1
	v_cndmask_b32_e32 v200, v178, v16, vcc
	v_cmp_lt_u32_e32 vcc, v157, v76
	s_nop 1
	v_cndmask_b32_e32 v76, v178, v17, vcc
	v_max3_f32 v3, v3, v200, v76
	s_nop 0
	v_max3_f32 v2, v2, v3, v3
	s_nop 0
	v_mov_b32_e32 v3, v2
	s_nop 1
	v_permlane32_swap_b32_e32 v2, v3
	v_max_f32_e32 v3, v3, v3
	v_max_f32_e32 v2, v2, v2
	v_max_f32_e32 v2, v2, v3
	v_cndmask_b32_e64 v201, v2, 0, s[10:11]
	v_sub_f32_e32 v2, v50, v201
	v_exp_f32_e32 v2, v2
	v_sub_f32_e32 v3, v51, v201
	v_exp_f32_e32 v3, v3
	v_sub_f32_e32 v4, v52, v201
	v_exp_f32_e32 v4, v4
	v_sub_f32_e32 v5, v53, v201
	v_exp_f32_e32 v5, v5
	v_add_f32_e32 v6, 0, v2
	v_add_f32_e32 v6, v3, v6
	v_add_f32_e32 v6, v4, v6
	v_add_f32_e32 v14, v5, v6
	v_sub_f32_e32 v6, v54, v201
	v_exp_f32_e32 v6, v6
	v_sub_f32_e32 v7, v55, v201
	v_exp_f32_e32 v7, v7
	v_sub_f32_e32 v12, v56, v201
	v_exp_f32_e32 v12, v12
	v_sub_f32_e32 v13, v57, v201
	v_exp_f32_e32 v13, v13
	v_add_f32_e32 v14, v6, v14
	v_add_f32_e32 v14, v7, v14
	v_add_f32_e32 v14, v12, v14
	v_add_f32_e32 v18, v13, v14
	v_sub_f32_e32 v14, v58, v201
	v_exp_f32_e32 v14, v14
	v_sub_f32_e32 v15, v59, v201
	v_exp_f32_e32 v15, v15
	v_sub_f32_e32 v16, v60, v201
	v_exp_f32_e32 v16, v16
	v_sub_f32_e32 v17, v61, v201
	v_exp_f32_e32 v17, v17
	v_add_f32_e32 v18, v14, v18
	v_add_f32_e32 v18, v15, v18
	v_add_f32_e32 v18, v16, v18
	v_add_f32_e32 v22, v17, v18
	v_sub_f32_e32 v18, v62, v201
	v_exp_f32_e32 v18, v18
	v_sub_f32_e32 v19, v63, v201
	v_exp_f32_e32 v19, v19
	v_sub_f32_e32 v20, v64, v201
	v_exp_f32_e32 v20, v20
	v_sub_f32_e32 v21, v65, v201
	v_exp_f32_e32 v21, v21
	v_add_f32_e32 v22, v18, v22
	v_add_f32_e32 v22, v19, v22
	v_add_f32_e32 v22, v20, v22
	v_add_f32_e32 v30, v21, v22
	v_sub_f32_e32 v22, v34, v201
	v_exp_f32_e32 v22, v22
	v_sub_f32_e32 v23, v35, v201
	v_exp_f32_e32 v23, v23
	v_sub_f32_e32 v28, v36, v201
	v_exp_f32_e32 v28, v28
	v_sub_f32_e32 v29, v37, v201
	v_exp_f32_e32 v29, v29
	v_add_f32_e32 v30, v22, v30
	v_add_f32_e32 v30, v23, v30
	v_add_f32_e32 v30, v28, v30
	v_add_f32_e32 v36, v29, v30
	v_sub_f32_e32 v30, v38, v201
	v_exp_f32_e32 v30, v30
	v_sub_f32_e32 v31, v39, v201
	v_exp_f32_e32 v31, v31
	v_sub_f32_e32 v34, v40, v201
	v_exp_f32_e32 v34, v34
	v_sub_f32_e32 v35, v41, v201
	v_exp_f32_e32 v35, v35
	v_add_f32_e32 v36, v30, v36
	v_add_f32_e32 v36, v31, v36
	v_add_f32_e32 v36, v34, v36
	v_add_f32_e32 v40, v35, v36
	v_sub_f32_e32 v36, v42, v201
	v_exp_f32_e32 v36, v36
	v_sub_f32_e32 v37, v43, v201
	v_exp_f32_e32 v37, v37
	v_sub_f32_e32 v38, v44, v201
	v_exp_f32_e32 v38, v38
	v_sub_f32_e32 v39, v45, v201
	v_exp_f32_e32 v39, v39
	v_add_f32_e32 v40, v36, v40
	v_add_f32_e32 v40, v37, v40
	v_add_f32_e32 v40, v38, v40
	v_add_f32_e32 v44, v39, v40
	v_sub_f32_e32 v40, v46, v201
	v_exp_f32_e32 v40, v40
	v_sub_f32_e32 v41, v47, v201
	v_exp_f32_e32 v41, v41
	v_sub_f32_e32 v42, v48, v201
	v_exp_f32_e32 v42, v42
	v_sub_f32_e32 v43, v49, v201
	v_exp_f32_e32 v43, v43
	v_add_f32_e32 v44, v40, v44
	v_add_f32_e32 v44, v41, v44
	v_add_f32_e32 v44, v42, v44
	v_add_f32_e32 v48, v43, v44
	v_sub_f32_e32 v44, v87, v201
	v_exp_f32_e32 v44, v44
	v_sub_f32_e32 v45, v89, v201
	v_exp_f32_e32 v45, v45
	v_sub_f32_e32 v46, v91, v201
	v_exp_f32_e32 v46, v46
	v_sub_f32_e32 v47, v92, v201
	v_exp_f32_e32 v47, v47
	v_add_f32_e32 v48, v44, v48
	v_add_f32_e32 v48, v45, v48
	v_add_f32_e32 v48, v46, v48
	v_add_f32_e32 v52, v47, v48
	v_sub_f32_e32 v48, v93, v201
	v_exp_f32_e32 v48, v48
	v_sub_f32_e32 v49, v94, v201
	v_exp_f32_e32 v49, v49
	v_sub_f32_e32 v24, v24, v201
	v_exp_f32_e32 v50, v24
	v_sub_f32_e32 v24, v25, v201
	v_exp_f32_e32 v51, v24
	v_sub_f32_e32 v25, v26, v201
	v_add_f32_e32 v24, v48, v52
	v_exp_f32_e32 v52, v25
	v_sub_f32_e32 v25, v27, v201
	v_add_f32_e32 v24, v49, v24
	v_exp_f32_e32 v53, v25
	v_sub_f32_e32 v25, v95, v201
	v_add_f32_e32 v24, v50, v24
	v_exp_f32_e32 v54, v25
	v_sub_f32_e32 v25, v96, v201
	v_add_f32_e32 v24, v51, v24
	v_exp_f32_e32 v55, v25
	v_sub_f32_e32 v25, v97, v201
	v_add_f32_e32 v24, v52, v24
	v_exp_f32_e32 v182, v25
	v_sub_f32_e32 v25, v183, v201
	v_add_f32_e32 v24, v53, v24
	v_exp_f32_e32 v183, v25
	v_sub_f32_e32 v25, v32, v201
	v_add_f32_e32 v24, v54, v24
	v_exp_f32_e32 v184, v25
	v_sub_f32_e32 v25, v33, v201
	v_add_f32_e32 v24, v55, v24
	v_exp_f32_e32 v185, v25
	v_sub_f32_e32 v25, v186, v201
	v_add_f32_e32 v24, v182, v24
	v_exp_f32_e32 v186, v25
	v_sub_f32_e32 v25, v187, v201
	v_add_f32_e32 v24, v183, v24
	v_exp_f32_e32 v187, v25
	v_sub_f32_e32 v25, v188, v201
	v_add_f32_e32 v24, v184, v24
	v_exp_f32_e32 v188, v25
	v_sub_f32_e32 v25, v189, v201
	v_add_f32_e32 v24, v185, v24
	v_exp_f32_e32 v189, v25
	v_sub_f32_e32 v25, v190, v201
	v_add_f32_e32 v24, v186, v24
	v_exp_f32_e32 v190, v25
	v_sub_f32_e32 v25, v191, v201
	v_add_f32_e32 v24, v187, v24
	v_exp_f32_e32 v191, v25
	v_sub_f32_e32 v8, v8, v201
	v_add_f32_e32 v24, v188, v24
	v_exp_f32_e32 v192, v8
	v_sub_f32_e32 v8, v9, v201
	v_add_f32_e32 v24, v189, v24
	v_exp_f32_e32 v193, v8
	v_sub_f32_e32 v9, v10, v201
	v_add_f32_e32 v8, v190, v24
	v_exp_f32_e32 v194, v9
	v_sub_f32_e32 v9, v11, v201
	v_add_f32_e32 v8, v191, v8
	v_exp_f32_e32 v195, v9
	v_sub_f32_e32 v9, v196, v201
	v_add_f32_e32 v8, v192, v8
	v_exp_f32_e32 v196, v9
	v_sub_f32_e32 v9, v197, v201
	v_add_f32_e32 v8, v193, v8
	v_exp_f32_e32 v197, v9
	v_sub_f32_e32 v9, v198, v201
	v_add_f32_e32 v8, v194, v8
	v_exp_f32_e32 v198, v9
	v_sub_f32_e32 v9, v199, v201
	v_add_f32_e32 v8, v195, v8
	v_exp_f32_e32 v199, v9
	v_sub_f32_e32 v9, v200, v201
	v_add_f32_e32 v8, v196, v8
	v_exp_f32_e32 v200, v9
	v_sub_f32_e32 v9, v76, v201
	v_add_f32_e32 v8, v197, v8
	v_exp_f32_e32 v201, v9
	v_add_f32_e32 v8, v198, v8
	v_add_f32_e32 v8, v199, v8
	v_add_f32_e32 v8, v200, v8
	v_add_f32_e32 v8, v201, v8
	v_mov_b32_e32 v9, v8
	s_nop 1
	v_permlane32_swap_b32_e32 v8, v9
	v_add_f32_e32 v8, v8, v9
	v_div_scale_f32 v9, s[40:41], v8, v8, 1.0
	v_rcp_f32_e32 v10, v9
	s_add_i32 s40, s31, 0
	s_add_i32 s40, s40, 0x10a00
	v_fma_f32 v11, -v9, v10, 1.0
	v_fmac_f32_e32 v10, v11, v10
	v_div_scale_f32 v11, vcc, 1.0, v8, 1.0
	v_mul_f32_e32 v24, v11, v10
	v_fma_f32 v25, -v9, v24, v11
	v_fmac_f32_e32 v24, v25, v10
	v_fma_f32 v9, -v9, v24, v11
	v_div_fmas_f32 v9, v9, v10, v24
	v_div_fixup_f32 v8, v9, v8, 1.0
	v_cndmask_b32_e64 v76, v8, 0, s[10:11]
	v_pk_mul_f32 v[10:11], v[76:77], v[2:3] op_sel_hi:[0,1]
	v_pk_mul_f32 v[8:9], v[76:77], v[4:5] op_sel_hi:[0,1]
	v_pk_mul_f32 v[6:7], v[76:77], v[6:7] op_sel_hi:[0,1]
	v_pk_mul_f32 v[4:5], v[76:77], v[12:13] op_sel_hi:[0,1]
	v_add_f32_e32 v12, v8, v9
	v_add_f32_e32 v13, v10, v11
	v_pk_mul_f32 v[2:3], v[76:77], v[14:15] op_sel_hi:[0,1]
	v_pk_mul_f32 v[24:25], v[76:77], v[16:17] op_sel_hi:[0,1]
	v_add_f32_e32 v12, v13, v12
	v_add_f32_e32 v13, v4, v5
	v_add_f32_e32 v14, v6, v7
	v_pk_mul_f32 v[26:27], v[76:77], v[18:19] op_sel_hi:[0,1]
	v_pk_mul_f32 v[32:33], v[76:77], v[20:21] op_sel_hi:[0,1]
	v_add_f32_e32 v13, v14, v13
	v_add_f32_e32 v14, v24, v25
	v_add_f32_e32 v15, v2, v3
	v_pk_mul_f32 v[92:93], v[76:77], v[22:23] op_sel_hi:[0,1]
	v_pk_mul_f32 v[94:95], v[76:77], v[28:29] op_sel_hi:[0,1]
	v_add_f32_e32 v14, v15, v14
	v_add_f32_e32 v15, v32, v33
	v_add_f32_e32 v16, v26, v27
	v_pk_mul_f32 v[96:97], v[76:77], v[30:31] op_sel_hi:[0,1]
	v_pk_mul_f32 v[28:29], v[76:77], v[34:35] op_sel_hi:[0,1]
	v_add_f32_e32 v15, v16, v15
	v_add_f32_e32 v16, v94, v95
	v_add_f32_e32 v17, v92, v93
	v_pk_mul_f32 v[30:31], v[76:77], v[36:37] op_sel_hi:[0,1]
	v_pk_mul_f32 v[18:19], v[76:77], v[38:39] op_sel_hi:[0,1]
	v_pk_mul_f32 v[20:21], v[76:77], v[40:41] op_sel_hi:[0,1]
	v_pk_mul_f32 v[22:23], v[76:77], v[42:43] op_sel_hi:[0,1]
	v_pk_mul_f32 v[64:65], v[76:77], v[44:45] op_sel_hi:[0,1]
	v_pk_mul_f32 v[62:63], v[76:77], v[46:47] op_sel_hi:[0,1]
	v_pk_mul_f32 v[60:61], v[76:77], v[48:49] op_sel_hi:[0,1]
	v_pk_mul_f32 v[58:59], v[76:77], v[50:51] op_sel_hi:[0,1]
	v_pk_mul_f32 v[56:57], v[76:77], v[52:53] op_sel_hi:[0,1]
	v_pk_mul_f32 v[40:41], v[76:77], v[54:55] op_sel_hi:[0,1]
	v_pk_mul_f32 v[42:43], v[76:77], v[182:183] op_sel_hi:[0,1]
	v_pk_mul_f32 v[48:49], v[76:77], v[184:185] op_sel_hi:[0,1]
	v_pk_mul_f32 v[50:51], v[76:77], v[186:187] op_sel_hi:[0,1]
	v_pk_mul_f32 v[52:53], v[76:77], v[188:189] op_sel_hi:[0,1]
	v_pk_mul_f32 v[54:55], v[76:77], v[190:191] op_sel_hi:[0,1]
	v_pk_mul_f32 v[44:45], v[76:77], v[192:193] op_sel_hi:[0,1]
	v_pk_mul_f32 v[46:47], v[76:77], v[194:195] op_sel_hi:[0,1]
	v_pk_mul_f32 v[34:35], v[76:77], v[196:197] op_sel_hi:[0,1]
	v_pk_mul_f32 v[36:37], v[76:77], v[198:199] op_sel_hi:[0,1]
	v_pk_mul_f32 v[38:39], v[76:77], v[200:201] op_sel_hi:[0,1]
	v_add_f32_e32 v16, v17, v16
	v_add_f32_e32 v17, v28, v29
	v_add_f32_e32 v76, v96, v97
	v_add_f32_e32 v17, v76, v17
	v_add_f32_e32 v76, v18, v19
	v_add_f32_e32 v87, v30, v31
	v_add_f32_e32 v76, v87, v76
	v_add_f32_e32 v87, v22, v23
	v_add_f32_e32 v89, v20, v21
	v_add_f32_e32 v87, v89, v87
	v_add_f32_e32 v89, v62, v63
	v_add_f32_e32 v91, v64, v65
	v_add_f32_e32 v89, v91, v89
	v_add_f32_e32 v91, v58, v59
	v_add_f32_e32 v182, v60, v61
	v_add_f32_e32 v91, v182, v91
	v_add_f32_e32 v182, v40, v41
	v_add_f32_e32 v183, v56, v57
	v_add_f32_e32 v182, v183, v182
	v_add_f32_e32 v183, v48, v49
	v_add_f32_e32 v184, v42, v43
	v_add_f32_e32 v183, v184, v183
	v_add_f32_e32 v184, v52, v53
	v_add_f32_e32 v185, v50, v51
	v_add_f32_e32 v184, v185, v184
	v_add_f32_e32 v185, v44, v45
	v_add_f32_e32 v186, v54, v55
	v_add_f32_e32 v185, v186, v185
	v_add_f32_e32 v186, v34, v35
	v_add_f32_e32 v187, v46, v47
	v_add_f32_e32 v186, v187, v186
	v_add_f32_e32 v187, v38, v39
	v_add_f32_e32 v188, v36, v37
	v_add_f32_e32 v187, v188, v187
	v_mov_b32_e32 v188, v9
	v_mov_b32_e32 v189, v9
	s_nop 1
	v_permlane32_swap_b32_e32 v188, v189
	v_cndmask_b32_e64 v188, v188, v189, s[2:3]
	v_cndmask_b32_e64 v189, v188, 0, s[4:5]
	v_add_f32_e32 v12, v189, v12
	v_mov_b32_e32 v189, v5
	v_mov_b32_e32 v190, v5
	s_nop 1
	v_permlane32_swap_b32_e32 v189, v190
	v_cndmask_b32_e64 v189, v189, v190, s[2:3]
	v_cndmask_b32_e64 v188, v189, v188, s[4:5]
	v_add_f32_e32 v188, v188, v13
	v_mov_b32_e32 v13, v25
	v_mov_b32_e32 v190, v25
	s_nop 1
	v_permlane32_swap_b32_e32 v13, v190
	v_cndmask_b32_e64 v13, v13, v190, s[2:3]
	v_cndmask_b32_e64 v189, v13, v189, s[4:5]
	v_add_f32_e32 v189, v189, v14
	v_mov_b32_e32 v14, v33
	v_mov_b32_e32 v190, v33
	s_nop 1
	v_permlane32_swap_b32_e32 v14, v190
	v_cndmask_b32_e64 v14, v14, v190, s[2:3]
	v_cndmask_b32_e64 v13, v14, v13, s[4:5]
	v_add_f32_e32 v190, v15, v13
	v_mov_b32_e32 v13, v95
	v_mov_b32_e32 v15, v95
	s_nop 1
	v_permlane32_swap_b32_e32 v13, v15
	v_cndmask_b32_e64 v13, v13, v15, s[2:3]
	v_cndmask_b32_e64 v14, v13, v14, s[4:5]
	v_add_f32_e32 v191, v16, v14
	v_mov_b32_e32 v14, v29
	v_mov_b32_e32 v15, v29
	s_nop 1
	v_permlane32_swap_b32_e32 v14, v15
	v_cndmask_b32_e64 v14, v14, v15, s[2:3]
	v_cndmask_b32_e64 v13, v14, v13, s[4:5]
	v_add_f32_e32 v192, v17, v13
	v_mov_b32_e32 v13, v19
	v_mov_b32_e32 v15, v19
	s_nop 1
	v_permlane32_swap_b32_e32 v13, v15
	v_cndmask_b32_e64 v13, v13, v15, s[2:3]
	v_cndmask_b32_e64 v14, v13, v14, s[4:5]
	v_add_f32_e32 v193, v76, v14
	v_mov_b32_e32 v14, v23
	v_mov_b32_e32 v15, v23
	s_nop 1
	v_permlane32_swap_b32_e32 v14, v15
	v_cndmask_b32_e64 v14, v14, v15, s[2:3]
	v_cndmask_b32_e64 v13, v14, v13, s[4:5]
	v_add_f32_e32 v194, v87, v13
	v_mov_b32_e32 v13, v63
	v_mov_b32_e32 v15, v63
	s_nop 1
	v_permlane32_swap_b32_e32 v13, v15
	v_cndmask_b32_e64 v13, v13, v15, s[2:3]
	v_cndmask_b32_e64 v14, v13, v14, s[4:5]
	v_add_f32_e32 v195, v89, v14
	v_mov_b32_e32 v14, v59
	v_mov_b32_e32 v15, v59
	s_nop 1
	v_permlane32_swap_b32_e32 v14, v15
	v_cndmask_b32_e64 v14, v14, v15, s[2:3]
	v_cndmask_b32_e64 v13, v14, v13, s[4:5]
	v_add_f32_e32 v196, v91, v13
	v_mov_b32_e32 v13, v41
	v_mov_b32_e32 v15, v41
	s_nop 1
	v_permlane32_swap_b32_e32 v13, v15
	v_cndmask_b32_e64 v13, v13, v15, s[2:3]
	v_cndmask_b32_e64 v14, v13, v14, s[4:5]
	v_add_f32_e32 v197, v182, v14
	v_mov_b32_e32 v14, v49
	v_mov_b32_e32 v15, v49
	s_nop 1
	v_permlane32_swap_b32_e32 v14, v15
	v_cndmask_b32_e64 v14, v14, v15, s[2:3]
	v_cndmask_b32_e64 v13, v14, v13, s[4:5]
	v_add_f32_e32 v198, v183, v13
	v_mov_b32_e32 v13, v53
	v_mov_b32_e32 v15, v53
	s_nop 1
	v_permlane32_swap_b32_e32 v13, v15
	v_cndmask_b32_e64 v13, v13, v15, s[2:3]
	v_cndmask_b32_e64 v14, v13, v14, s[4:5]
	v_add_f32_e32 v199, v184, v14
	v_mov_b32_e32 v14, v45
	v_mov_b32_e32 v15, v45
	s_nop 1
	v_permlane32_swap_b32_e32 v14, v15
	v_cndmask_b32_e64 v14, v14, v15, s[2:3]
	v_cndmask_b32_e64 v13, v14, v13, s[4:5]
	v_add_f32_e32 v200, v185, v13
	v_mov_b32_e32 v13, v35
	v_mov_b32_e32 v15, v35
	s_nop 1
	v_permlane32_swap_b32_e32 v13, v15
	v_cndmask_b32_e64 v13, v13, v15, s[2:3]
	v_cndmask_b32_e64 v14, v13, v14, s[4:5]
	v_add_f32_e32 v201, v186, v14
	v_mov_b32_e32 v14, v39
	v_mov_b32_e32 v15, v39
	s_nop 1
	v_permlane32_swap_b32_e32 v14, v15
	v_cndmask_b32_e64 v14, v14, v15, s[2:3]
	v_cndmask_b32_e64 v13, v14, v13, s[4:5]
	v_add_f32_e32 v202, v187, v13
	v_add_f32_dpp v12, v12, v12 quad_perm:[1,0,3,2] row_mask:0xf bank_mask:0xf bound_ctrl:1
	v_mov_b32_e32 v13, v77
	v_add_f32_dpp v14, v188, v188 quad_perm:[1,0,3,2] row_mask:0xf bank_mask:0xf bound_ctrl:1
	v_mov_b32_e32 v15, v77
	v_add_f32_dpp v16, v189, v189 quad_perm:[1,0,3,2] row_mask:0xf bank_mask:0xf bound_ctrl:1
	v_mov_b32_e32 v17, v77
	v_add_f32_dpp v76, v190, v190 quad_perm:[1,0,3,2] row_mask:0xf bank_mask:0xf bound_ctrl:1
	v_mov_b32_e32 v87, v77
	v_add_f32_dpp v89, v191, v191 quad_perm:[1,0,3,2] row_mask:0xf bank_mask:0xf bound_ctrl:1
	v_mov_b32_e32 v91, v77
	v_add_f32_dpp v182, v192, v192 quad_perm:[1,0,3,2] row_mask:0xf bank_mask:0xf bound_ctrl:1
	v_mov_b32_e32 v183, v77
	v_add_f32_dpp v184, v193, v193 quad_perm:[1,0,3,2] row_mask:0xf bank_mask:0xf bound_ctrl:1
	v_mov_b32_e32 v185, v77
	v_add_f32_dpp v186, v194, v194 quad_perm:[1,0,3,2] row_mask:0xf bank_mask:0xf bound_ctrl:1
	v_mov_b32_e32 v187, v77
	v_add_f32_dpp v188, v195, v195 quad_perm:[1,0,3,2] row_mask:0xf bank_mask:0xf bound_ctrl:1
	v_mov_b32_e32 v189, v77
	v_add_f32_dpp v190, v196, v196 quad_perm:[1,0,3,2] row_mask:0xf bank_mask:0xf bound_ctrl:1
	v_mov_b32_e32 v191, v77
	v_add_f32_dpp v192, v197, v197 quad_perm:[1,0,3,2] row_mask:0xf bank_mask:0xf bound_ctrl:1
	v_mov_b32_e32 v193, v77
	v_add_f32_dpp v194, v198, v198 quad_perm:[1,0,3,2] row_mask:0xf bank_mask:0xf bound_ctrl:1
	v_mov_b32_e32 v195, v77
	v_add_f32_dpp v196, v199, v199 quad_perm:[1,0,3,2] row_mask:0xf bank_mask:0xf bound_ctrl:1
	v_mov_b32_e32 v197, v77
	v_add_f32_dpp v198, v200, v200 quad_perm:[1,0,3,2] row_mask:0xf bank_mask:0xf bound_ctrl:1
	v_mov_b32_e32 v199, v77
	v_add_f32_dpp v200, v201, v201 quad_perm:[1,0,3,2] row_mask:0xf bank_mask:0xf bound_ctrl:1
	v_mov_b32_e32 v201, v77
	v_add_f32_dpp v202, v202, v202 quad_perm:[1,0,3,2] row_mask:0xf bank_mask:0xf bound_ctrl:1
	v_mov_b32_dpp v13, v12 quad_perm:[2,3,0,1] row_mask:0xf bank_mask:0xf
	v_mov_b32_dpp v15, v14 quad_perm:[2,3,0,1] row_mask:0xf bank_mask:0xf
	v_mov_b32_dpp v17, v16 quad_perm:[2,3,0,1] row_mask:0xf bank_mask:0xf
	v_mov_b32_dpp v87, v76 quad_perm:[2,3,0,1] row_mask:0xf bank_mask:0xf
	v_mov_b32_dpp v91, v89 quad_perm:[2,3,0,1] row_mask:0xf bank_mask:0xf
	v_mov_b32_dpp v183, v182 quad_perm:[2,3,0,1] row_mask:0xf bank_mask:0xf
	v_mov_b32_dpp v185, v184 quad_perm:[2,3,0,1] row_mask:0xf bank_mask:0xf
	v_mov_b32_dpp v187, v186 quad_perm:[2,3,0,1] row_mask:0xf bank_mask:0xf
	v_mov_b32_dpp v189, v188 quad_perm:[2,3,0,1] row_mask:0xf bank_mask:0xf
	v_mov_b32_dpp v191, v190 quad_perm:[2,3,0,1] row_mask:0xf bank_mask:0xf
	v_mov_b32_dpp v193, v192 quad_perm:[2,3,0,1] row_mask:0xf bank_mask:0xf
	v_mov_b32_dpp v195, v194 quad_perm:[2,3,0,1] row_mask:0xf bank_mask:0xf
	v_mov_b32_dpp v197, v196 quad_perm:[2,3,0,1] row_mask:0xf bank_mask:0xf
	v_mov_b32_dpp v199, v198 quad_perm:[2,3,0,1] row_mask:0xf bank_mask:0xf
	v_mov_b32_dpp v201, v200 quad_perm:[2,3,0,1] row_mask:0xf bank_mask:0xf
	v_mov_b32_dpp v203, v202 quad_perm:[2,3,0,1] row_mask:0xf bank_mask:0xf
	s_and_saveexec_b64 s[10:11], s[6:7]
	s_cbranch_execz .LBB0_556
	v_add_f32_e32 v12, v12, v13
	v_lshlrev_b32_e32 v13, 2, v74
	v_add_f32_e32 v14, v14, v15
	v_add3_u32 v13, s40, v158, v13
	v_add_f32_e32 v202, v202, v203
	v_add_f32_e32 v200, v200, v201
	v_add_f32_e32 v198, v198, v199
	v_add_f32_e32 v196, v196, v197
	v_add_f32_e32 v194, v194, v195
	v_add_f32_e32 v192, v192, v193
	v_add_f32_e32 v190, v190, v191
	v_add_f32_e32 v188, v188, v189
	v_add_f32_e32 v186, v186, v187
	v_add_f32_e32 v184, v184, v185
	v_add_f32_e32 v182, v182, v183
	v_add_f32_e32 v89, v89, v91
	v_add_f32_e32 v76, v76, v87
	v_add_f32_e32 v16, v16, v17
	ds_write2_b32 v13, v12, v14 offset1:2
	ds_write2_b32 v13, v16, v76 offset0:4 offset1:6
	ds_write2_b32 v13, v89, v182 offset0:8 offset1:10
	ds_write2_b32 v13, v184, v186 offset0:12 offset1:14
	ds_write2_b32 v13, v188, v190 offset0:16 offset1:18
	ds_write2_b32 v13, v192, v194 offset0:20 offset1:22
	ds_write2_b32 v13, v196, v198 offset0:24 offset1:26
	ds_write2_b32 v13, v200, v202 offset0:28 offset1:30

.LBB0_637:
	s_waitcnt lgkmcnt(0)
	s_barrier
	s_and_saveexec_b64 s[2:3], s[0:1]
	s_cbranch_execz .LBB0_641
	s_waitcnt lgkmcnt(0)
	s_cmp_eq_u32 s100, 4
	s_cbranch_scc1 .Lqp4_have
	s_waitcnt vmcnt(0)
	v_mov_b32_e32 v253, 1
	global_atomic_add v253, v163, v253, s[92:93] offset:512 sc0
	s_waitcnt vmcnt(0)
	s_branch .Lqp4_go

.Lqp4_go:
	v_mov_b32_e32 v3, s38
	ds_write_b32 v3, v253
	s_waitcnt lgkmcnt(0)
	v_mov_b32_e32 v253, 1
	global_atomic_add v253, v163, v253, s[92:93] offset:512 sc0
.LBB0_641:
	s_or_b64 exec, exec, s[2:3]
	s_mov_b32 s100, 4
	s_waitcnt lgkmcnt(0)
	s_barrier
	ds_read_b32 v2, v172
	s_mov_b64 s[2:3], -1
	s_waitcnt lgkmcnt(0)
	v_cmp_le_i32_e32 vcc, s15, v2
	v_readfirstlane_b32 s6, v2
	s_cbranch_vccnz .LBB0_636
	s_add_i32 s2, s6, 0xfffffe00
	s_cmpk_gt_i32 s6, 0x1ff
	s_cselect_b32 s2, s2, s6
	s_ashr_i32 s3, s2, 31
	s_lshr_b32 s3, s3, 26
	s_add_i32 s3, s2, s3
	s_ashr_i32 s10, s3, 6
	s_andn2_b32 s3, s3, 63
	v_mov_b32_e32 v14, v0
	s_sub_i32 s11, s2, s3
	s_and_b32 s2, s11, 3
	v_readfirstlane_b32 s43, v14
	s_ashr_i32 s41, s43, 6
	s_sub_i32 s44, 7, s10
	s_ashr_i32 s45, s43, 8
	s_and_b32 s12, s41, 3
	s_lshl_b32 s2, s2, 1
	s_ashr_i32 s8, s11, 2
	s_add_i32 s33, s45, s2
	s_lshl_b32 s2, s44, 8
	s_lshl_b32 s54, s12, 6
	s_ashr_i32 s9, s8, 31
	s_or_b32 s42, s54, s2
	s_lshl_b32 s2, s33, 6
	s_ashr_i32 s3, s2, 31
	s_lshl_b64 s[6:7], s[8:9], 21
	v_and_b32_e32 v177, 31, v14
	s_add_u32 s13, s16, s6
	v_or_b32_e32 v162, s42, v177
	s_addc_u32 s46, s17, s7
	s_lshl_b64 s[6:7], s[2:3], 1
	v_or_b32_e32 v164, 32, v162
	s_add_u32 s2, s13, s6
	v_mov_b32_e32 v165, v163
	s_addc_u32 s3, s46, s7
	v_lshlrev_b64 v[2:3], 10, v[162:163]
	v_lshlrev_b64 v[6:7], 10, v[164:165]
	v_lshl_add_u64 v[2:3], s[2:3], 0, v[2:3]
	v_lshl_add_u64 v[6:7], s[2:3], 0, v[6:7]
	s_lshl_b32 s2, s8, 1
	s_bfe_u32 s11, s11, 0x10001
	s_or_b32 s2, s11, s2
	s_ashr_i32 s3, s2, 31
	v_bfe_u32 v176, v14, 5, 1
	s_lshl_b64 s[2:3], s[2:3], 13
	v_lshlrev_b32_e32 v4, 4, v176
	v_mov_b32_e32 v5, v163
	s_add_u32 s2, s18, s2
	v_lshl_add_u64 v[6:7], v[6:7], 0, v[4:5]
	s_addc_u32 s3, s19, s3
	v_lshl_add_u64 v[2:3], v[2:3], 0, v[4:5]
	v_lshl_add_u64 v[8:9], v[162:163], 2, s[2:3]
	global_load_dwordx4 v[130:133], v[6:7], off offset:96
	global_load_dwordx4 v[138:141], v[6:7], off offset:64
	global_load_dwordx4 v[134:137], v[2:3], off offset:96
	global_load_dwordx4 v[142:145], v[2:3], off offset:64
	global_load_dwordx4 v[146:149], v[6:7], off offset:32
	global_load_dwordx4 v[154:157], v[6:7], off
	global_load_dwordx4 v[150:153], v[2:3], off offset:32
	global_load_dwordx4 v[158:161], v[2:3], off
	global_load_dword v184, v[8:9], off
	global_load_dword v183, v[8:9], off offset:128
	v_lshlrev_b32_e32 v6, 6, v14
	v_and_b32_e32 v6, 0xf00, v6
	v_lshl_or_b32 v6, s12, 12, v6
	s_lshl_b64 s[12:13], s[8:9], 19
	s_lshl_b32 s11, s11, 7
	s_or_b32 s55, s12, s11
	s_add_u32 s2, s20, s55
	v_and_b32_e32 v180, 63, v14
	s_addc_u32 s3, s21, s13
	v_mov_b32_e32 v3, v163
	v_lshlrev_b32_e32 v2, 8, v180
	s_add_u32 s46, s22, s55
	v_lshl_add_u64 v[10:11], s[2:3], 0, v[2:3]
	s_addc_u32 s47, s23, s13
	s_lshl_b32 s2, s41, 3
	s_lshl_b32 s48, s45, 5
	v_mov_b32_e32 v7, v163
	v_lshlrev_b32_e32 v178, 3, v14
	s_lshl_b32 s45, s41, 10
	s_ashr_i32 s3, s2, 31
	s_ashr_i32 s49, s48, 31
	v_and_b32_e32 v16, 24, v178
	v_lshl_add_u64 v[12:13], s[46:47], 0, v[6:7]
	s_add_i32 s45, s45, 0
	s_lshl_b64 s[50:51], s[2:3], 1
	s_lshl_b64 s[52:53], s[48:49], 1
	v_mov_b32_e32 v15, v163
	v_mov_b32_e32 v9, v163
	v_lshlrev_b32_e32 v8, 1, v16
	s_add_i32 s2, s45, 0x8000
	v_lshl_add_u64 v[10:11], v[10:11], 0, s[50:51]
	v_lshl_add_u64 v[12:13], v[12:13], 0, s[52:53]
	s_mov_b32 m0, s45
	v_lshl_add_u64 v[8:9], v[12:13], 0, v[8:9]
	v_lshlrev_b32_e32 v179, 2, v176
	s_lshl_b32 s49, s10, 2
	s_lshl_b32 s10, s10, 8
	s_sub_i32 s10, s54, s10
	s_or_b32 s48, s42, 63
	s_sub_i32 s49, 31, s49
	s_addk_i32 s10, 0x700
	v_mov_b32_e32 v34, v163
	v_mov_b32_e32 v35, v163
	v_mov_b32_e32 v48, v163
	v_mov_b32_e32 v49, v163
	v_mov_b32_e32 v36, v163
	v_mov_b32_e32 v37, v163
	v_mov_b32_e32 v38, v163
	v_mov_b32_e32 v39, v163
	s_waitcnt vmcnt(0)
	s_barrier
	global_load_lds_dwordx4 v[10:11], off
	s_mov_b32 m0, s2
	s_and_b32 s2, s43, 0x3fffffc0
	global_load_lds_dwordx4 v[8:9], off
	s_lshl_b32 s2, s2, 2
	s_add_i32 s2, s2, 0
	v_lshlrev_b32_e32 v5, 1, v14
	v_lshrrev_b32_e32 v8, 2, v14
	s_add_i32 s43, s2, 0x10400
	v_and_b32_e32 v5, 32, v5
	v_and_or_b32 v8, v8, 3, v179
	v_lshlrev_b32_e32 v8, 6, v8
	v_lshl_add_u32 v174, v177, 2, s43
	v_add_u32_e32 v165, s43, v4
	s_or_b32 s43, s42, 32
	v_add_u32_e32 v4, 0, v5
	v_add3_u32 v182, v4, v8, v16
	v_or_b32_e32 v4, s10, v177
	s_add_u32 s10, s34, s50
	s_addc_u32 s50, s35, s51
	s_add_u32 s10, s10, s11
	s_addc_u32 s11, s50, 0
	s_add_u32 s10, s10, s12
	s_addc_u32 s11, s11, s13
	v_lshl_add_u64 v[166:167], s[10:11], 0, v[2:3]
	s_add_u32 s10, s52, s55
	v_and_b32_e32 v2, 3, v14
	s_addc_u32 s11, s53, s13
	v_lshl_or_b32 v2, v2, 4, s10
	v_mov_b32_e32 v3, s11
	s_waitcnt vmcnt(0)
	v_lshlrev_b32_e32 v9, 10, v176
	v_lshlrev_b32_e32 v10, 4, v177
	v_lshl_add_u64 v[2:3], v[2:3], 0, v[6:7]
	v_add3_u32 v185, 0, v9, v10
	v_sub_u32_e32 v188, v4, v179
	v_lshl_add_u64 v[168:169], s[4:5], 0, v[2:3]
	v_mov_b32_e32 v40, v163
	v_mov_b32_e32 v41, v163
	v_mov_b32_e32 v42, v163
	v_mov_b32_e32 v43, v163
	v_mov_b32_e32 v44, v163
	v_mov_b32_e32 v45, v163
	v_mov_b32_e32 v46, v163
	v_mov_b32_e32 v47, v163
	v_mov_b64_e32 v[64:65], v[48:49]
	v_mov_b64_e32 v[2:3], v[34:35]
	v_mov_b64_e32 v[18:19], v[34:35]
	s_mov_b32 s46, 63
	s_mov_b32 s47, 0
	v_or_b32_e32 v186, v184, v183
	v_cmp_gt_u32_e64 s[2:3], 32, v180
	v_mov_b32_e32 v189, 0
	s_mov_b64 s[10:11], 0
	v_mov_b64_e32 v[62:63], v[46:47]
	v_mov_b64_e32 v[60:61], v[44:45]
	v_mov_b64_e32 v[58:59], v[42:43]
	v_mov_b64_e32 v[56:57], v[40:41]
	v_mov_b64_e32 v[54:55], v[38:39]
	v_mov_b64_e32 v[52:53], v[36:37]
	v_mov_b64_e32 v[50:51], v[34:35]
	v_mov_b64_e32 v[4:5], v[36:37]
	v_mov_b64_e32 v[6:7], v[38:39]
	v_mov_b64_e32 v[8:9], v[40:41]
	v_mov_b64_e32 v[10:11], v[42:43]
	v_mov_b64_e32 v[12:13], v[44:45]
	v_mov_b64_e32 v[14:15], v[46:47]
	v_mov_b64_e32 v[16:17], v[48:49]
	v_mov_b64_e32 v[20:21], v[36:37]
	v_mov_b64_e32 v[22:23], v[38:39]
	v_mov_b64_e32 v[24:25], v[40:41]
	v_mov_b64_e32 v[26:27], v[42:43]
	v_mov_b64_e32 v[28:29], v[44:45]
	v_mov_b64_e32 v[30:31], v[46:47]
	v_mov_b64_e32 v[32:33], v[48:49]
	v_mov_b32_e32 v181, 0
	v_mov_b32_e32 v187, 0
	v_mov_b32_e32 v175, 0
	s_waitcnt vmcnt(0) lgkmcnt(0)
	s_barrier
	s_branch .LBB0_646
